# speedup vs baseline: 1.0220x; 1.0072x over previous
.LBB0_3:
	s_cmpk_gt_u32 s2, 0x7ff
	s_cbranch_scc0 .LBB0_7
	s_load_dwordx2 s[10:11], s[0:1], 0x8
	s_load_dwordx2 s[4:5], s[0:1], 0x20
	s_add_i32 s3, s2, 0xfffff800
	s_lshl_b32 s12, s3, 14
	v_lshrrev_b32_e32 v1, 6, v0
	v_and_b32_e32 v2, 63, v0
	v_lshlrev_b32_e32 v3, 12, v1
	v_lshl_or_b32 v3, v2, 4, v3
	v_lshlrev_b32_e32 v4, 7, v1
	v_and_b32_e32 v5, 15, v2
	v_lshl_or_b32 v4, v5, 3, v4
	v_lshrrev_b32_e32 v5, 4, v2
	v_lshl_or_b32 v4, v5, 22, v4
	s_waitcnt lgkmcnt(0)
	s_add_u32 s10, s10, s12
	s_addc_u32 s11, s11, 0
	global_load_dwordx4 v[8:11], v3, s[10:11] nt
	global_load_dwordx4 v[12:15], v3, s[10:11] offset:1024 nt
	global_load_dwordx4 v[16:19], v3, s[10:11] offset:2048 nt
	global_load_dwordx4 v[20:23], v3, s[10:11] offset:3072 nt
	s_lshl_b32 s13, s3, 9
	s_add_u32 s4, s4, s13
	s_addc_u32 s5, s5, 0
	s_add_u32 s6, s4, 0x1000000
	s_addc_u32 s7, s5, 0
	s_add_u32 s8, s4, 0x2000000
	s_addc_u32 s9, s5, 0
	s_add_u32 s12, s4, 0x3000000
	s_addc_u32 s13, s5, 0
	s_mov_b32 s14, 0x4038aa3b
	s_waitcnt vmcnt(3)
	v_pk_mul_f32 v[8:9], v[8:9], s[14:15] op_sel_hi:[1,0]
	v_pk_mul_f32 v[10:11], v[10:11], s[14:15] op_sel_hi:[1,0]
	v_cvt_pk_bf16_f32 v8, v8, v9
	v_cvt_pk_bf16_f32 v9, v10, v11
	global_store_dwordx2 v4, v[8:9], s[4:5]
	s_waitcnt vmcnt(3)
	v_pk_mul_f32 v[12:13], v[12:13], s[14:15] op_sel_hi:[1,0]
	v_pk_mul_f32 v[14:15], v[14:15], s[14:15] op_sel_hi:[1,0]
	v_cvt_pk_bf16_f32 v12, v12, v13
	v_cvt_pk_bf16_f32 v13, v14, v15
	global_store_dwordx2 v4, v[12:13], s[6:7]
	s_waitcnt vmcnt(3)
	v_pk_mul_f32 v[16:17], v[16:17], s[14:15] op_sel_hi:[1,0]
	v_pk_mul_f32 v[18:19], v[18:19], s[14:15] op_sel_hi:[1,0]
	v_cvt_pk_bf16_f32 v16, v16, v17
	v_cvt_pk_bf16_f32 v17, v18, v19
	global_store_dwordx2 v4, v[16:17], s[8:9]
	s_waitcnt vmcnt(3)
	v_pk_mul_f32 v[20:21], v[20:21], s[14:15] op_sel_hi:[1,0]
	v_pk_mul_f32 v[22:23], v[22:23], s[14:15] op_sel_hi:[1,0]
	v_cvt_pk_bf16_f32 v20, v20, v21
	v_cvt_pk_bf16_f32 v21, v22, v23
	global_store_dwordx2 v4, v[20:21], s[12:13]
	s_endpgm
